# hand-rewritten pipelined k3 loop + sc1 write-through stores + early/pre-barrier L2 warm-up
# speedup vs baseline: 1.0466x; 1.0070x over previous
.LBB2_414:
	s_movk_i32 s0, 0xc00
	v_mov_b64_e32 v[26:27], s[42:43]
	v_mul_u32_u24_e32 v28, 0xc00, v154
	v_mad_i64_i32 v[26:27], s[0:1], v62, s0, v[26:27]
	v_or_b32_e32 v28, v28, v98
	v_mov_b32_e32 v99, 0
	v_lshl_add_u64 v[26:27], v[26:27], 0, v[98:99]
	v_or_b32_e32 v29, 0x10000, v28
	global_store_dwordx4 v[26:27], v[22:25], off sc1
	ds_write_b128 v29, v[22:25]
	v_sub_f32_e32 v10, v10, v22
	v_or_b32_e32 v22, v101, v154
	v_sub_f32_e32 v11, v11, v23
	v_add_u32_e32 v23, v22, v102
	v_lshl_or_b32 v23, v23, 4, v103
	ds_write_b32 v23, v10
	v_add_u32_e32 v10, v22, v104
	v_lshl_or_b32 v10, v10, 4, v105
	ds_write_b32 v10, v11
	v_or_b32_e32 v10, v106, v154
	v_add_u32_e32 v10, v10, v107
	v_sub_f32_e32 v12, v12, v24
	v_lshl_or_b32 v10, v10, 4, v108
	ds_write_b32 v10, v12
	v_or_b32_e32 v10, v109, v154
	v_add_u32_e32 v10, v10, v110
	v_sub_f32_e32 v13, v13, v25
	v_lshl_or_b32 v10, v10, 4, v111
	ds_write_b32 v10, v13
	v_add_u32_e32 v10, 0x10400, v28
	ds_write_b128 v10, v[18:21]
	v_sub_f32_e32 v10, v6, v18
	v_sub_f32_e32 v11, v7, v19
	v_pk_add_f32 v[6:7], v[8:9], v[20:21] neg_lo:[0,1] neg_hi:[0,1]
	v_or_b32_e32 v8, v112, v154
	v_add_u32_e32 v9, v8, v113
	v_add_u32_e32 v8, v8, v115
	v_lshl_or_b32 v9, v9, 4, v114
	v_lshl_or_b32 v8, v8, 4, v116
	ds_write_b32 v9, v10
	ds_write_b32 v8, v11
	v_or_b32_e32 v8, v117, v154
	v_add_u32_e32 v8, v8, v118
	v_lshl_or_b32 v8, v8, 4, v119
	ds_write_b32 v8, v6
	v_or_b32_e32 v6, v120, v154
	v_add_u32_e32 v6, v6, v121
	v_lshl_or_b32 v6, v6, 4, v122
	ds_write_b32 v6, v7
	v_add_u32_e32 v6, 0x10800, v28
	ds_write_b128 v6, v[14:17]
	v_or_b32_e32 v6, v123, v154
	v_add_u32_e32 v7, v6, v124
	v_pk_add_f32 v[2:3], v[2:3], v[14:15] neg_lo:[0,1] neg_hi:[0,1]
	v_lshl_or_b32 v7, v7, 4, v125
	ds_write_b32 v7, v2
	v_add_u32_e32 v2, v6, v126
	v_lshl_or_b32 v2, v2, 4, v127
	ds_write_b32 v2, v3
	v_or_b32_e32 v2, v133, v154
	v_add_u32_e32 v2, v2, v134
	v_pk_add_f32 v[4:5], v[4:5], v[16:17] neg_lo:[0,1] neg_hi:[0,1]
	v_lshl_or_b32 v2, v2, 4, v63
	ds_write_b32 v2, v4
	v_or_b32_e32 v2, v135, v154
	v_add_u32_e32 v2, v2, v132
	v_lshl_or_b32 v2, v2, 4, v136
	v_add_lshl_u32 v4, v100, v154, 4
	s_mov_b32 s5, 0
	s_mov_b32 s4, 1.0
	ds_write_b32 v2, v5
	v_mov_b64_e32 v[2:3], s[4:5]
	v_add_u32_e32 v4, 8, v4
	s_waitcnt vmcnt(1)
	v_lshlrev_b32_e32 v40, 9, v150
	ds_write2st64_b64 v4, v[2:3], v[2:3] offset1:64
	v_or_b32_e32 v2, v40, v128
	v_lshlrev_b32_e32 v98, 4, v2
	v_lshl_add_u64 v[100:101], s[40:41], 0, v[98:99]
	s_mov_b64 s[0:1], 0x787000
	v_lshl_add_u64 v[34:35], v[100:101], 0, s[0:1]
	s_mov_b32 s0, 0x788000
	v_add_co_u32_e32 v36, vcc, s0, v100
	global_store_dwordx4 v[26:27], v[18:21], off offset:1024 sc1
	global_store_dwordx4 v[26:27], v[14:17], off offset:2048 sc1
	s_lshr_b32 s59, s33, 4
	s_and_b32 s59, s59, 31
	s_lshl_b32 s59, s59, 15
	s_add_u32 s59, s59, 0x787000
	s_add_u32 s68, s40, s59
	s_addc_u32 s69, s41, 0
	v_lshlrev_b32_e32 v207, 6, v0
	global_load_dword v207, v207, s[68:69]
	s_waitcnt lgkmcnt(0)
	s_barrier
	v_addc_co_u32_e32 v37, vcc, 0, v101, vcc
	global_load_dwordx4 v[2:5], v[34:35], off offset:1024
	global_load_dwordx4 v[10:13], v[34:35], off offset:2048
	global_load_dwordx4 v[14:17], v[34:35], off offset:3072
	global_load_dwordx4 v[6:9], v[36:37], off offset:-4096
	global_load_dwordx4 v[18:21], v[36:37], off
	global_load_dwordx4 v[22:25], v[36:37], off offset:1024
	global_load_dwordx4 v[26:29], v[36:37], off offset:2048
	global_load_dwordx4 v[30:33], v[36:37], off offset:3072
	v_and_b32_e32 v35, 15, v0
	v_lshrrev_b32_e32 v37, 4, v128
	v_lshlrev_b32_e32 v102, 2, v35
	v_lshlrev_b32_e32 v41, 2, v37
	v_lshlrev_b32_e32 v34, 4, v35
	v_cmp_gt_u32_e64 s[0:1], 6, v35
	v_mov_b32_e32 v35, v99
	v_or3_b32 v36, v34, v41, v40
	v_lshl_add_u64 v[104:105], s[44:45], 0, v[34:35]
	v_or_b32_e32 v34, v40, v34
	s_movk_i32 s4, 0x1000
	v_or3_b32 v153, v34, v41, s4
	v_or_b32_e32 v34, 0x11800, v98
	v_lshl_add_u64 v[118:119], s[40:41], 0, v[34:35]
	v_or_b32_e32 v34, 0x11400, v98
	v_lshl_add_u64 v[120:121], s[40:41], 0, v[34:35]
	v_or_b32_e32 v34, 0x11000, v98
	ds_read2st64_b32 v[132:133], v36 offset1:1
	v_or_b32_e32 v36, s33, v41
	v_lshl_add_u64 v[122:123], s[40:41], 0, v[34:35]
	v_or_b32_e32 v34, 0x10c00, v98
	v_or_b32_e32 v38, 1, v36
	v_lshl_add_u64 v[124:125], s[40:41], 0, v[34:35]
	v_or_b32_e32 v34, 0x10800, v98
	v_mul_u32_u24_e32 v152, 0x3000, v37
	v_ashrrev_i32_e32 v37, 31, v36
	v_ashrrev_i32_e32 v39, 31, v38
	v_lshl_add_u64 v[126:127], s[40:41], 0, v[34:35]
	v_or_b32_e32 v34, 0x10400, v98
	v_mov_b32_e32 v103, v99
	v_lshlrev_b64 v[108:109], 17, v[36:37]
	v_lshlrev_b64 v[110:111], 17, v[38:39]
	v_or_b32_e32 v38, 2, v36
	v_or_b32_e32 v36, 3, v36
	v_lshl_add_u64 v[128:129], s[40:41], 0, v[34:35]
	v_mul_u32_u24_e32 v34, 24, v150
	v_lshl_add_u64 v[106:107], s[38:39], 0, v[102:103]
	v_ashrrev_i32_e32 v39, 31, v38
	v_ashrrev_i32_e32 v37, 31, v36
	v_lshlrev_b32_e32 v103, 2, v0
	v_or_b32_e32 v98, 0x11c00, v98
	v_or_b32_e32 v34, v152, v34
	v_lshlrev_b64 v[112:113], 17, v[38:39]
	v_lshlrev_b64 v[114:115], 17, v[36:37]
	v_and_b32_e32 v116, 0x700, v103
	v_mov_b32_e32 v117, v99
	v_lshl_add_u64 v[130:131], s[40:41], 0, v[98:99]
	v_add_u32_e32 v154, v34, v102
	s_mov_b64 s[6:7], 0
	s_mov_b64 s[8:9], 0x800
	v_mov_b32_e32 v155, 0x400
	v_mov_b32_e32 v159, 0
	v_mov_b32_e32 v158, 0
	v_mov_b32_e32 v157, 0
	v_mov_b32_e32 v156, 0
	v_readfirstlane_b32 s78, v150
	v_and_b32_e32 v104, 63, v0
	v_lshlrev_b32_e32 v104, 4, v104
	v_lshl_or_b32 v104, v150, 13, v104
	v_add_u32_e32 v105, 0xfffff000, v153
	v_mov_b32_e32 v106, v154
	v_lshrrev_b32_e32 v98, 2, v102
	v_cmp_gt_u32_e32 vcc, 6, v98
	v_add_u32_e32 v107, -6, v98
	s_nop 0
	v_cndmask_b32_e32 v107, v107, v98, vcc
	v_cmp_gt_u32_e32 vcc, 6, v107
	v_add_u32_e32 v98, -6, v107
	s_nop 0
	v_cndmask_b32_e32 v107, v98, v107, vcc
	v_lshlrev_b32_e32 v107, 2, v107
	v_sub_u32_e32 v106, v106, v102
	v_add_u32_e32 v106, v106, v107
	v_and_b32_e32 v98, 63, v0
	v_lshrrev_b32_e32 v98, 4, v98
	v_lshlrev_b32_e32 v98, 19, v98
	v_lshl_or_b32 v108, v102, 2, v98
	v_add_u32_e32 v109, 0x20000, v108
	v_add_u32_e32 v110, 0x40000, v108
	v_add_u32_e32 v111, 0x60000, v108
	v_mov_b32_e32 v240, 0
	v_mov_b32_e32 v241, 0
	v_mov_b32_e32 v242, 0
	v_mov_b32_e32 v243, 0
	s_lshl_b32 s84, s33, 17
	s_lshl_b32 s85, s78, 10
	s_add_u32 s84, s84, s85
	s_add_u32 s80, s44, s84
	s_addc_u32 s81, s45, 0
	s_mul_i32 s84, s78, 0x1800
	s_add_u32 s94, s38, s84
	s_addc_u32 s95, s39, 0
	s_mov_b32 s70, 0
	s_add_u32 s86, s40, 0x797000
	s_addc_u32 s87, s41, 0
	s_add_u32 s88, s86, 0x1000
	s_addc_u32 s89, s87, 0
	v_add_u32_e32 v112, 0x1000, v105
	s_waitcnt vmcnt(0) lgkmcnt(0)
	v_mfma_f32_16x16x4_f32 v[34:37], v132, v6, 0
	v_mfma_f32_16x16x4_f32 v[38:41], v132, v8, 0
	v_mfma_f32_16x16x4_f32 v[34:37], v133, v7, v[34:37]
	v_mfma_f32_16x16x4_f32 v[38:41], v133, v9, v[38:41]
	global_load_dwordx4 v[6:9], v104, s[86:87]
	v_mfma_f32_16x16x4_f32 v[42:45], v132, v2, 0
	v_mfma_f32_16x16x4_f32 v[46:49], v132, v4, 0
	v_mfma_f32_16x16x4_f32 v[42:45], v133, v3, v[42:45]
	v_mfma_f32_16x16x4_f32 v[46:49], v133, v5, v[46:49]
	global_load_dwordx4 v[2:5], v104, s[86:87] offset:1024
	v_mfma_f32_16x16x4_f32 v[50:53], v132, v10, 0
	v_mfma_f32_16x16x4_f32 v[54:57], v132, v12, 0
	v_mfma_f32_16x16x4_f32 v[50:53], v133, v11, v[50:53]
	v_mfma_f32_16x16x4_f32 v[54:57], v133, v13, v[54:57]
	global_load_dwordx4 v[10:13], v104, s[86:87] offset:2048
	v_mfma_f32_16x16x4_f32 v[58:61], v132, v14, 0
	v_mfma_f32_16x16x4_f32 v[62:65], v132, v16, 0
	v_mfma_f32_16x16x4_f32 v[58:61], v133, v15, v[58:61]
	v_mfma_f32_16x16x4_f32 v[62:65], v133, v17, v[62:65]
	global_load_dwordx4 v[14:17], v104, s[86:87] offset:3072
	v_mfma_f32_16x16x4_f32 v[66:69], v132, v18, 0
	v_mfma_f32_16x16x4_f32 v[70:73], v132, v20, 0
	v_mfma_f32_16x16x4_f32 v[66:69], v133, v19, v[66:69]
	v_mfma_f32_16x16x4_f32 v[70:73], v133, v21, v[70:73]
	global_load_dwordx4 v[18:21], v104, s[88:89]
	v_mfma_f32_16x16x4_f32 v[74:77], v132, v22, 0
	v_mfma_f32_16x16x4_f32 v[78:81], v132, v24, 0
	v_mfma_f32_16x16x4_f32 v[74:77], v133, v23, v[74:77]
	v_mfma_f32_16x16x4_f32 v[78:81], v133, v25, v[78:81]
	global_load_dwordx4 v[22:25], v104, s[88:89] offset:1024
	v_mfma_f32_16x16x4_f32 v[82:85], v132, v26, 0
	v_mfma_f32_16x16x4_f32 v[86:89], v132, v28, 0
	v_mfma_f32_16x16x4_f32 v[82:85], v133, v27, v[82:85]
	v_mfma_f32_16x16x4_f32 v[86:89], v133, v29, v[86:89]
	global_load_dwordx4 v[26:29], v104, s[88:89] offset:2048
	v_mfma_f32_16x16x4_f32 v[90:93], v132, v30, 0
	v_mfma_f32_16x16x4_f32 v[94:97], v132, v32, 0
	v_mfma_f32_16x16x4_f32 v[90:93], v133, v31, v[90:93]
	v_mfma_f32_16x16x4_f32 v[94:97], v133, v33, v[94:97]
	global_load_dwordx4 v[30:33], v104, s[88:89] offset:3072
	ds_read2st64_b32 v[132:133], v112 offset1:1
	s_nop 7
	s_nop 7
	v_max3_f32 v114, v34, v38, v42
	v_max3_f32 v116, v46, v50, v54
	v_max3_f32 v114, v114, v58, v62
	v_max3_f32 v116, v116, v66, v70
	v_max3_f32 v114, v114, v74, v78
	v_max3_f32 v116, v116, v82, v86
	v_max3_f32 v114, v114, v90, v94
	v_max_f32_e32 v114, v114, v116
	s_nop 1
	v_max_f32_dpp v114, v114, v114 row_ror:1 row_mask:0xf bank_mask:0xf
	s_nop 1
	v_max_f32_dpp v114, v114, v114 row_ror:2 row_mask:0xf bank_mask:0xf
	s_nop 1
	v_max_f32_dpp v114, v114, v114 row_ror:4 row_mask:0xf bank_mask:0xf
	s_nop 1
	v_max_f32_dpp v114, v114, v114 row_ror:8 row_mask:0xf bank_mask:0xf
	s_waitcnt vmcnt(0) lgkmcnt(0)
